# speedup vs baseline: 1.0837x; 1.0245x over previous
.LBB1_162:
	v_lshrrev_b32_e32 v15, 15, v14
	v_and_b32_e32 v15, 0x1fffc, v15
	v_add_u32_e32 v16, 0x22000, v15
	ds_add_rtn_u32 v16, v16, v4
	v_add_u32_e32 v15, 0x22800, v15
	ds_read_b32 v15, v15
	v_and_b32_e32 v17, 0x1ffff, v14
	s_waitcnt lgkmcnt(0)
	v_add_u32_e32 v14, v16, v15
	v_lshlrev_b32_e32 v14, 2, v14
	ds_write_b32 v14, v17
	s_or_b64 exec, exec, s[14:15]
	v_cmp_lt_i32_e32 vcc, -1, v13
	s_and_saveexec_b64 s[14:15], vcc
	s_cbranch_execz .LBB1_155
.LBB1_163:
	v_lshrrev_b32_e32 v14, 15, v13
	v_and_b32_e32 v14, 0x1fffc, v14
	v_add_u32_e32 v15, 0x22000, v14
	ds_add_rtn_u32 v15, v15, v4
	v_add_u32_e32 v14, 0x22800, v14
	ds_read_b32 v14, v14
	v_and_b32_e32 v13, 0x1ffff, v13
	s_waitcnt lgkmcnt(0)
	v_add_u32_e32 v14, v15, v14
	v_lshlrev_b32_e32 v14, 2, v14
	ds_write_b32 v14, v13
	s_or_b64 exec, exec, s[14:15]
	v_cmp_lt_i32_e32 vcc, -1, v11
	s_and_saveexec_b64 s[14:15], vcc
	s_cbranch_execz .LBB1_156
.LBB1_164:
	v_lshrrev_b32_e32 v13, 15, v11
	v_and_b32_e32 v13, 0x1fffc, v13
	v_add_u32_e32 v14, 0x22000, v13
	ds_add_rtn_u32 v14, v14, v4
	v_add_u32_e32 v13, 0x22800, v13
	ds_read_b32 v13, v13
	v_and_b32_e32 v11, 0x1ffff, v11
	s_waitcnt lgkmcnt(0)
	v_add_u32_e32 v14, v14, v13
	v_lshlrev_b32_e32 v14, 2, v14
	ds_write_b32 v14, v11
	s_or_b64 exec, exec, s[14:15]
	v_cmp_lt_i32_e32 vcc, -1, v12
	s_and_saveexec_b64 s[14:15], vcc
	s_cbranch_execz .LBB1_157
.LBB1_165:
	v_lshrrev_b32_e32 v11, 15, v12
	v_and_b32_e32 v11, 0x1fffc, v11
	v_add_u32_e32 v13, 0x22000, v11
	ds_add_rtn_u32 v13, v13, v4
	v_add_u32_e32 v11, 0x22800, v11
	ds_read_b32 v11, v11
	v_and_b32_e32 v14, 0x1ffff, v12
	s_waitcnt lgkmcnt(0)
	v_add_u32_e32 v12, v13, v11
	v_lshlrev_b32_e32 v12, 2, v12
	ds_write_b32 v12, v14
	s_or_b64 exec, exec, s[14:15]
	v_cmp_lt_i32_e32 vcc, -1, v9
	s_and_saveexec_b64 s[14:15], vcc
	s_cbranch_execz .LBB1_158
.LBB1_166:
	v_lshrrev_b32_e32 v11, 15, v9
	v_and_b32_e32 v11, 0x1fffc, v11
	v_add_u32_e32 v12, 0x22000, v11
	ds_add_rtn_u32 v12, v12, v4
	v_add_u32_e32 v11, 0x22800, v11
	ds_read_b32 v11, v11
	v_and_b32_e32 v9, 0x1ffff, v9
	s_waitcnt lgkmcnt(0)
	v_add_u32_e32 v12, v12, v11
	v_lshlrev_b32_e32 v12, 2, v12
	ds_write_b32 v12, v9
	s_or_b64 exec, exec, s[14:15]
	v_cmp_lt_i32_e32 vcc, -1, v10
	s_and_saveexec_b64 s[14:15], vcc
	s_cbranch_execz .LBB1_159
.LBB1_167:
	v_lshrrev_b32_e32 v9, 15, v10
	v_and_b32_e32 v9, 0x1fffc, v9
	v_add_u32_e32 v11, 0x22000, v9
	ds_add_rtn_u32 v11, v11, v4
	v_add_u32_e32 v9, 0x22800, v9
	ds_read_b32 v9, v9
	v_and_b32_e32 v12, 0x1ffff, v10
	s_waitcnt lgkmcnt(0)
	v_add_u32_e32 v10, v11, v9
	v_lshlrev_b32_e32 v10, 2, v10
	ds_write_b32 v10, v12
	s_or_b64 exec, exec, s[14:15]
	v_cmp_lt_i32_e32 vcc, -1, v5
	s_and_saveexec_b64 s[14:15], vcc
	s_cbranch_execz .LBB1_160
.LBB1_168:
	v_lshrrev_b32_e32 v9, 15, v5
	v_and_b32_e32 v9, 0x1fffc, v9
	v_add_u32_e32 v10, 0x22000, v9
	ds_add_rtn_u32 v10, v10, v4
	v_add_u32_e32 v9, 0x22800, v9
	ds_read_b32 v9, v9
	v_and_b32_e32 v5, 0x1ffff, v5
	s_waitcnt lgkmcnt(0)
	v_add_u32_e32 v10, v10, v9
	v_lshlrev_b32_e32 v10, 2, v10
	ds_write_b32 v10, v5
	s_or_b64 exec, exec, s[14:15]
	s_waitcnt vmcnt(1)
	v_cmp_lt_i32_e32 vcc, -1, v8
	s_and_saveexec_b64 s[14:15], vcc
	s_cbranch_execz .LBB1_139
.LBB1_169:
	v_lshrrev_b32_e32 v5, 15, v8
	v_and_b32_e32 v5, 0x1fffc, v5
	v_add_u32_e32 v9, 0x22000, v5
	ds_add_rtn_u32 v9, v9, v4
	v_add_u32_e32 v5, 0x22800, v5
	ds_read_b32 v5, v5
	v_and_b32_e32 v10, 0x1ffff, v8
	s_waitcnt lgkmcnt(0)
	v_add_u32_e32 v8, v9, v5
	v_lshlrev_b32_e32 v8, 2, v8
	ds_write_b32 v8, v10
	s_branch .LBB1_139
.LBB1_170:
	s_or_b64 exec, exec, s[4:5]
	s_cbranch_execz .LBB1_56
	s_waitcnt lgkmcnt(0)
	s_barrier
	v_mov_b32_e32 v2, 0x227fc
	v_mov_b32_e32 v3, 0x22ffc
	ds_read_b32 v2, v2
	ds_read_b32 v3, v3
	v_lshlrev_b32_e32 v8, 2, v0
	v_add_u32_e32 v4, v6, v0
	v_ashrrev_i32_e32 v5, 31, v4
	v_lshl_add_u64 v[4:5], v[4:5], 2, s[12:13]
	v_mov_b32_e32 v9, v0
	s_mov_b64 s[24:25], 0x1000
	s_mov_b32 s21, 0
	s_waitcnt lgkmcnt(0)
	v_add_u32_e32 v2, v2, v3
	s_nop 0
	v_readfirstlane_b32 s20, v2
.Lmy_csr_copy:
	s_cmp_ge_i32 s21, s20
	s_cbranch_scc1 .LBB1_171
	v_cmp_gt_i32_e32 vcc, s20, v9
	s_and_saveexec_b64 s[22:23], vcc
	s_cbranch_execz .Lmy_csr_skip
	ds_read_b32 v7, v8
	s_waitcnt lgkmcnt(0)
	global_store_dword v[4:5], v7, off
.Lmy_csr_skip:
	s_or_b64 exec, exec, s[22:23]
	v_add_u32_e32 v9, 0x400, v9
	v_add_u32_e32 v8, 0x1000, v8
	v_lshl_add_u64 v[4:5], v[4:5], 0, s[24:25]
	s_addk_i32 s21, 0x400
	s_branch .Lmy_csr_copy
